# P13 gather loop: wait for the previous batch before issuing the next batch of table gathers (fewer loads queued per wave); second measurement
# speedup vs baseline: 1.0177x; 1.0063x over previous
.LBB0_1456:
	v_lshl_add_u32 v3, s0, 9, v162
	ds_read2_b32 v[4:5], v3 offset0:64 offset1:68
	ds_read2_b32 v[78:79], v3 offset0:72 offset1:76
	v_mov_b32_e32 v177, 0
	s_waitcnt vmcnt(2)
	v_dot4c_i32_i8_e32 v177, v6, v10
	v_dot4c_i32_i8_e32 v177, v7, v11
	s_waitcnt lgkmcnt(1)
	v_lshl_or_b32 v4, v4, 8, v144
	v_lshl_or_b32 v5, v5, 8, v144
	s_waitcnt vmcnt(0)
	global_load_dwordx4 v[138:141], v4, s[26:27]
	global_load_dwordx4 v[134:137], v5, s[26:27]
	ds_read2_b32 v[4:5], v3 offset0:80 offset1:84
	s_waitcnt lgkmcnt(1)
	v_lshl_or_b32 v78, v78, 8, v144
	v_lshl_or_b32 v79, v79, 8, v144
	global_load_dwordx4 v[130:133], v78, s[26:27]
	global_load_dwordx4 v[122:125], v79, s[26:27]
	ds_read2_b32 v[78:79], v3 offset0:88 offset1:92
	s_waitcnt lgkmcnt(1)
	v_lshl_or_b32 v4, v4, 8, v144
	v_lshl_or_b32 v5, v5, 8, v144
	global_load_dwordx4 v[126:129], v4, s[26:27]
	global_load_dwordx4 v[118:121], v5, s[26:27]
	ds_read2_b32 v[4:5], v3 offset0:96 offset1:100
	s_waitcnt lgkmcnt(1)
	v_lshl_or_b32 v78, v78, 8, v144
	v_lshl_or_b32 v79, v79, 8, v144
	global_load_dwordx4 v[114:117], v78, s[26:27]
	global_load_dwordx4 v[106:109], v79, s[26:27]
	ds_read2_b32 v[78:79], v3 offset0:104 offset1:108
	s_waitcnt lgkmcnt(1)
	v_lshl_or_b32 v4, v4, 8, v144
	v_lshl_or_b32 v5, v5, 8, v144
	global_load_dwordx4 v[110:113], v4, s[26:27]
	global_load_dwordx4 v[102:105], v5, s[26:27]
	ds_read2_b32 v[4:5], v3 offset0:112 offset1:116
	s_waitcnt lgkmcnt(1)
	v_lshl_or_b32 v78, v78, 8, v144
	v_lshl_or_b32 v79, v79, 8, v144
	global_load_dwordx4 v[98:101], v78, s[26:27]
	global_load_dwordx4 v[90:93], v79, s[26:27]
	ds_read2_b32 v[78:79], v3 offset0:120 offset1:124
	s_waitcnt lgkmcnt(1)
	v_lshl_or_b32 v3, v4, 8, v144
	v_lshl_or_b32 v4, v5, 8, v144
	global_load_dwordx4 v[94:97], v3, s[26:27]
	global_load_dwordx4 v[86:89], v4, s[26:27]
	v_dot4c_i32_i8_e32 v177, v8, v12
	s_waitcnt lgkmcnt(0)
	v_lshl_or_b32 v3, v78, 8, v144
	v_lshl_or_b32 v4, v79, 8, v144
	global_load_dwordx4 v[82:85], v3, s[26:27]
	global_load_dwordx4 v[78:81], v4, s[26:27]
	s_waitcnt lgkmcnt(0)
	v_lshl_add_u32 v4, s36, 2, v162
	v_lshl_add_u32 v8, s36, 2, v162
	ds_read_b32 v6, v4
	v_dot4c_i32_i8_e32 v177, v9, v13
	ds_read_b32 v9, v8 offset:240
	ds_read2_b32 v[4:5], v8 offset0:4 offset1:8
	v_mov_b32_e32 v3, 0
	v_mov_b32_e32 v163, 0
	s_waitcnt vmcnt(16)
	v_dot4c_i32_i8_e32 v3, v74, v10
	v_dot4c_i32_i8_e32 v163, v70, v10
	v_dot4c_i32_i8_e32 v3, v75, v11
	v_dot4c_i32_i8_e32 v163, v71, v11
	v_mov_b32_e32 v176, 0
	v_dot4c_i32_i8_e32 v3, v76, v12
	v_dot4c_i32_i8_e32 v163, v72, v12
	v_dot4c_i32_i8_e32 v176, v14, v10
	s_waitcnt lgkmcnt(2)
	v_lshl_or_b32 v14, v6, 8, v144
	ds_read2_b32 v[6:7], v8 offset0:12 offset1:16
	s_waitcnt lgkmcnt(1)
	v_lshl_or_b32 v4, v4, 8, v144
	v_dot4c_i32_i8_e32 v3, v77, v13
	v_dot4c_i32_i8_e32 v163, v73, v13
	s_waitcnt vmcnt(0)
	global_load_dwordx4 v[74:77], v14, s[26:27]
	global_load_dwordx4 v[70:73], v4, s[26:27]
	v_lshl_or_b32 v14, v5, 8, v144
	ds_read2_b32 v[4:5], v8 offset0:20 offset1:24
	v_mov_b32_e32 v164, 0
	v_mov_b32_e32 v165, 0
	v_dot4c_i32_i8_e32 v164, v66, v10
	v_dot4c_i32_i8_e32 v165, v62, v10
	v_mov_b32_e32 v166, 0
	v_mov_b32_e32 v167, 0
	v_dot4c_i32_i8_e32 v164, v67, v11
	v_dot4c_i32_i8_e32 v165, v63, v11
	v_dot4c_i32_i8_e32 v166, v58, v10
	v_dot4c_i32_i8_e32 v167, v54, v10
	v_dot4c_i32_i8_e32 v164, v68, v12
	v_dot4c_i32_i8_e32 v165, v64, v12
	v_dot4c_i32_i8_e32 v166, v59, v11
	v_dot4c_i32_i8_e32 v167, v55, v11
	s_waitcnt lgkmcnt(1)
	v_lshl_or_b32 v6, v6, 8, v144
	v_dot4c_i32_i8_e32 v164, v69, v13
	v_dot4c_i32_i8_e32 v165, v65, v13
	v_dot4c_i32_i8_e32 v166, v60, v12
	v_dot4c_i32_i8_e32 v167, v56, v12
	s_waitcnt vmcnt(0)
	global_load_dwordx4 v[66:69], v14, s[26:27]
	global_load_dwordx4 v[62:65], v6, s[26:27]
	v_lshl_or_b32 v14, v7, 8, v144
	s_waitcnt lgkmcnt(0)
	v_lshl_or_b32 v4, v4, 8, v144
	ds_read2_b32 v[6:7], v8 offset0:28 offset1:32
	v_dot4c_i32_i8_e32 v166, v61, v13
	v_dot4c_i32_i8_e32 v167, v57, v13
	global_load_dwordx4 v[58:61], v14, s[26:27]
	global_load_dwordx4 v[54:57], v4, s[26:27]
	v_lshl_or_b32 v14, v5, 8, v144
	ds_read2_b32 v[4:5], v8 offset0:36 offset1:40
	v_mov_b32_e32 v168, 0
	v_mov_b32_e32 v169, 0
	v_dot4c_i32_i8_e32 v168, v50, v10
	v_dot4c_i32_i8_e32 v169, v46, v10
	v_mov_b32_e32 v170, 0
	v_mov_b32_e32 v171, 0
	v_dot4c_i32_i8_e32 v168, v51, v11
	v_dot4c_i32_i8_e32 v169, v47, v11
	v_dot4c_i32_i8_e32 v170, v42, v10
	v_dot4c_i32_i8_e32 v171, v38, v10
	v_dot4c_i32_i8_e32 v168, v52, v12
	v_dot4c_i32_i8_e32 v169, v48, v12
	v_dot4c_i32_i8_e32 v170, v43, v11
	v_dot4c_i32_i8_e32 v171, v39, v11
	s_waitcnt lgkmcnt(1)
	v_lshl_or_b32 v6, v6, 8, v144
	v_dot4c_i32_i8_e32 v168, v53, v13
	v_dot4c_i32_i8_e32 v169, v49, v13
	v_dot4c_i32_i8_e32 v170, v44, v12
	v_dot4c_i32_i8_e32 v171, v40, v12
	s_waitcnt vmcnt(0)
	global_load_dwordx4 v[50:53], v14, s[26:27]
	global_load_dwordx4 v[46:49], v6, s[26:27]
	v_lshl_or_b32 v14, v7, 8, v144
	s_waitcnt lgkmcnt(0)
	v_lshl_or_b32 v4, v4, 8, v144
	ds_read2_b32 v[6:7], v8 offset0:44 offset1:48
	v_dot4c_i32_i8_e32 v170, v45, v13
	v_dot4c_i32_i8_e32 v171, v41, v13
	global_load_dwordx4 v[42:45], v14, s[26:27]
	global_load_dwordx4 v[38:41], v4, s[26:27]
	v_lshl_or_b32 v14, v5, 8, v144
	ds_read2_b32 v[4:5], v8 offset0:52 offset1:56
	v_mov_b32_e32 v172, 0
	v_mov_b32_e32 v173, 0
	v_dot4c_i32_i8_e32 v172, v34, v10
	v_dot4c_i32_i8_e32 v173, v30, v10
	v_mov_b32_e32 v174, 0
	v_mov_b32_e32 v175, 0
	v_dot4c_i32_i8_e32 v172, v35, v11
	v_dot4c_i32_i8_e32 v173, v31, v11
	v_dot4c_i32_i8_e32 v174, v26, v10
	v_dot4c_i32_i8_e32 v175, v22, v10
	v_dot4c_i32_i8_e32 v172, v36, v12
	v_dot4c_i32_i8_e32 v173, v32, v12
	v_dot4c_i32_i8_e32 v174, v27, v11
	v_dot4c_i32_i8_e32 v175, v23, v11
	s_waitcnt lgkmcnt(1)
	v_lshl_or_b32 v6, v6, 8, v144
	v_dot4c_i32_i8_e32 v172, v37, v13
	v_dot4c_i32_i8_e32 v173, v33, v13
	v_dot4c_i32_i8_e32 v174, v28, v12
	v_dot4c_i32_i8_e32 v175, v24, v12
	v_dot4c_i32_i8_e32 v176, v15, v11
	s_waitcnt vmcnt(0)
	global_load_dwordx4 v[34:37], v14, s[26:27]
	global_load_dwordx4 v[30:33], v6, s[26:27]
	v_lshl_or_b32 v6, v7, 8, v144
	s_waitcnt lgkmcnt(0)
	v_lshl_or_b32 v4, v4, 8, v144
	v_dot4c_i32_i8_e32 v174, v29, v13
	v_dot4c_i32_i8_e32 v175, v25, v13
	v_dot4c_i32_i8_e32 v176, v16, v12
	global_load_dwordx4 v[26:29], v6, s[26:27]
	global_load_dwordx4 v[22:25], v4, s[26:27]
	v_lshl_or_b32 v4, v5, 8, v144
	v_dot4c_i32_i8_e32 v176, v17, v13
	v_lshl_or_b32 v5, v9, 8, v144
	global_load_dwordx4 v[14:17], v4, s[26:27]
	global_load_dwordx4 v[6:9], v5, s[26:27]
	v_mov_b32_e32 v5, 0
	s_waitcnt vmcnt(30)
	v_dot4c_i32_i8_e32 v5, v134, v10
	v_mov_b32_e32 v134, 0
	s_waitcnt vmcnt(29)
	v_dot4c_i32_i8_e32 v134, v130, v10
	v_mov_b32_e32 v130, 0
	s_waitcnt vmcnt(28)
	v_dot4c_i32_i8_e32 v130, v122, v10
	v_dot4c_i32_i8_e32 v130, v123, v11
	v_mov_b32_e32 v123, 0
	s_waitcnt vmcnt(26)
	v_dot4c_i32_i8_e32 v123, v118, v10
	v_mov_b32_e32 v118, 0
	s_waitcnt vmcnt(25)
	v_dot4c_i32_i8_e32 v118, v114, v10
	v_mov_b32_e32 v114, 0
	s_waitcnt vmcnt(24)
	v_dot4c_i32_i8_e32 v114, v106, v10
	v_dot4c_i32_i8_e32 v114, v107, v11
	v_mov_b32_e32 v107, 0
	s_waitcnt vmcnt(22)
	v_dot4c_i32_i8_e32 v107, v102, v10
	v_mov_b32_e32 v102, 0
	v_mov_b32_e32 v4, 0
	s_waitcnt vmcnt(21)
	v_dot4c_i32_i8_e32 v102, v98, v10
	v_mov_b32_e32 v98, 0
	v_dot4c_i32_i8_e32 v4, v138, v10
	s_waitcnt vmcnt(20)
	v_dot4c_i32_i8_e32 v98, v90, v10
	v_dot4c_i32_i8_e32 v4, v139, v11
	v_dot4c_i32_i8_e32 v5, v135, v11
	v_dot4c_i32_i8_e32 v98, v91, v11
	v_mov_b32_e32 v91, 0
	v_dot4c_i32_i8_e32 v4, v140, v12
	v_dot4c_i32_i8_e32 v5, v136, v12
	v_dot4c_i32_i8_e32 v134, v131, v11
	v_mov_b32_e32 v122, 0
	s_waitcnt vmcnt(18)
	v_dot4c_i32_i8_e32 v91, v86, v10
	v_mov_b32_e32 v86, 0
	v_dot4c_i32_i8_e32 v4, v141, v13
	v_dot4c_i32_i8_e32 v5, v137, v13
	v_dot4c_i32_i8_e32 v134, v132, v12
	v_dot4c_i32_i8_e32 v122, v126, v10
	v_mov_b32_e32 v106, 0
	v_mov_b32_e32 v90, 0
	s_waitcnt vmcnt(17)
	v_dot4c_i32_i8_e32 v86, v82, v10
	v_mov_b32_e32 v82, 0
	v_dot4c_i32_i8_e32 v134, v133, v13
	v_dot4c_i32_i8_e32 v130, v124, v12
	v_dot4c_i32_i8_e32 v122, v127, v11
	v_dot4c_i32_i8_e32 v106, v110, v10
	v_dot4c_i32_i8_e32 v90, v94, v10
	s_waitcnt vmcnt(16)
	v_dot4c_i32_i8_e32 v82, v78, v10
	v_cndmask_b32_e64 v10, v3, v4, s[6:7]
	v_cndmask_b32_e64 v3, v4, v3, s[6:7]
	v_cndmask_b32_e64 v4, v163, v5, s[6:7]
	v_cndmask_b32_e64 v5, v5, v163, s[6:7]
	v_dot4c_i32_i8_e32 v130, v125, v13
	v_dot4c_i32_i8_e32 v122, v128, v12
	v_dot4c_i32_i8_e32 v123, v119, v11
	v_add_u32_dpp v3, v10, v3 row_ror:8 row_mask:0xf bank_mask:0xf bound_ctrl:1
	v_add_u32_dpp v4, v4, v5 row_ror:8 row_mask:0xf bank_mask:0xf bound_ctrl:1
	v_cndmask_b32_e64 v5, v164, v134, s[6:7]
	v_cndmask_b32_e64 v10, v134, v164, s[6:7]
	v_dot4c_i32_i8_e32 v122, v129, v13
	v_dot4c_i32_i8_e32 v123, v120, v12
	v_dot4c_i32_i8_e32 v118, v115, v11
	v_dot4c_i32_i8_e32 v106, v111, v11
	v_dot4c_i32_i8_e32 v107, v103, v11
	v_dot4c_i32_i8_e32 v102, v99, v11
	v_dot4c_i32_i8_e32 v90, v95, v11
	v_dot4c_i32_i8_e32 v91, v87, v11
	v_dot4c_i32_i8_e32 v86, v83, v11
	v_dot4c_i32_i8_e32 v82, v79, v11
	v_add_u32_dpp v5, v5, v10 row_ror:8 row_mask:0xf bank_mask:0xf bound_ctrl:1
	v_cndmask_b32_e64 v10, v165, v130, s[6:7]
	v_cndmask_b32_e64 v11, v130, v165, s[6:7]
	v_dot4c_i32_i8_e32 v123, v121, v13
	v_dot4c_i32_i8_e32 v118, v116, v12
	v_dot4c_i32_i8_e32 v114, v108, v12
	v_dot4c_i32_i8_e32 v106, v112, v12
	v_dot4c_i32_i8_e32 v107, v104, v12
	v_dot4c_i32_i8_e32 v102, v100, v12
	v_dot4c_i32_i8_e32 v98, v92, v12
	v_dot4c_i32_i8_e32 v90, v96, v12
	v_dot4c_i32_i8_e32 v91, v88, v12
	v_dot4c_i32_i8_e32 v86, v84, v12
	v_dot4c_i32_i8_e32 v82, v80, v12
	v_add_u32_dpp v10, v10, v11 row_ror:8 row_mask:0xf bank_mask:0xf bound_ctrl:1
	v_cndmask_b32_e64 v11, v166, v122, s[6:7]
	v_cndmask_b32_e64 v12, v122, v166, s[6:7]
	v_dot4c_i32_i8_e32 v118, v117, v13
	v_dot4c_i32_i8_e32 v114, v109, v13
	v_dot4c_i32_i8_e32 v106, v113, v13
	v_dot4c_i32_i8_e32 v107, v105, v13
	v_dot4c_i32_i8_e32 v102, v101, v13
	v_dot4c_i32_i8_e32 v98, v93, v13
	v_dot4c_i32_i8_e32 v90, v97, v13
	v_dot4c_i32_i8_e32 v91, v89, v13
	v_dot4c_i32_i8_e32 v86, v85, v13
	v_dot4c_i32_i8_e32 v82, v81, v13
	v_add_u32_dpp v11, v11, v12 row_ror:8 row_mask:0xf bank_mask:0xf bound_ctrl:1
	v_cndmask_b32_e64 v12, v167, v123, s[6:7]
	v_cndmask_b32_e64 v13, v123, v167, s[6:7]
	v_cndmask_b32_e64 v78, v118, v168, s[6:7]
	v_cndmask_b32_e64 v79, v114, v169, s[6:7]
	v_add_u32_dpp v12, v12, v13 row_ror:8 row_mask:0xf bank_mask:0xf bound_ctrl:1
	v_cndmask_b32_e64 v13, v168, v118, s[6:7]
	v_cndmask_b32_e64 v80, v106, v170, s[6:7]
	v_cndmask_b32_e64 v81, v107, v171, s[6:7]
	v_add_u32_dpp v13, v13, v78 row_ror:8 row_mask:0xf bank_mask:0xf bound_ctrl:1
	v_cndmask_b32_e64 v78, v169, v114, s[6:7]
	v_cndmask_b32_e64 v83, v102, v172, s[6:7]
	v_cndmask_b32_e64 v84, v98, v173, s[6:7]
	v_add_u32_dpp v78, v78, v79 row_ror:8 row_mask:0xf bank_mask:0xf bound_ctrl:1
	v_cndmask_b32_e64 v79, v170, v106, s[6:7]
	v_cndmask_b32_e64 v85, v90, v174, s[6:7]
	v_cndmask_b32_e64 v87, v91, v175, s[6:7]
	v_add_u32_dpp v79, v79, v80 row_ror:8 row_mask:0xf bank_mask:0xf bound_ctrl:1
	v_cndmask_b32_e64 v80, v171, v107, s[6:7]
	s_xor_b32 s0, s0, 1
	v_lshl_add_u64 v[160:161], v[160:161], 0, s[22:23]
	v_add_u32_dpp v80, v80, v81 row_ror:8 row_mask:0xf bank_mask:0xf bound_ctrl:1
	v_cndmask_b32_e64 v81, v172, v102, s[6:7]
	s_andn2_b64 vcc, exec, s[28:29]
	s_mov_b32 s37, s5
	v_add_u32_dpp v81, v81, v83 row_ror:8 row_mask:0xf bank_mask:0xf bound_ctrl:1
	v_cndmask_b32_e64 v83, v173, v98, s[6:7]
	s_nop 1
	v_add_u32_dpp v83, v83, v84 row_ror:8 row_mask:0xf bank_mask:0xf bound_ctrl:1
	v_cndmask_b32_e64 v84, v174, v90, s[6:7]
	s_nop 1
	v_add_u32_dpp v84, v84, v85 row_ror:8 row_mask:0xf bank_mask:0xf bound_ctrl:1
	v_cndmask_b32_e64 v85, v175, v91, s[6:7]
	s_nop 1
	v_add_u32_dpp v85, v85, v87 row_ror:8 row_mask:0xf bank_mask:0xf bound_ctrl:1
	v_cndmask_b32_e64 v87, v176, v86, s[6:7]
	v_cndmask_b32_e64 v86, v86, v176, s[6:7]
	s_nop 1
	v_add_u32_dpp v86, v87, v86 row_ror:8 row_mask:0xf bank_mask:0xf bound_ctrl:1
	v_cndmask_b32_e64 v87, v177, v82, s[6:7]
	v_cndmask_b32_e64 v82, v82, v177, s[6:7]
	s_nop 1
	v_add_u32_dpp v82, v87, v82 row_ror:8 row_mask:0xf bank_mask:0xf bound_ctrl:1
	v_cndmask_b32_e64 v87, v3, v79, s[8:9]
	v_cndmask_b32_e64 v3, v79, v3, s[8:9]
	v_cndmask_b32_e64 v79, v4, v80, s[8:9]
	v_cndmask_b32_e64 v4, v80, v4, s[8:9]
	v_add_u32_dpp v3, v87, v3 row_half_mirror row_mask:0xf bank_mask:0xf bound_ctrl:1
	s_nop 0
	v_add_u32_dpp v4, v79, v4 row_half_mirror row_mask:0xf bank_mask:0xf bound_ctrl:1
	v_cndmask_b32_e64 v79, v5, v81, s[8:9]
	v_cndmask_b32_e64 v5, v81, v5, s[8:9]
	s_nop 1
	v_add_u32_dpp v5, v79, v5 row_half_mirror row_mask:0xf bank_mask:0xf bound_ctrl:1
	v_cndmask_b32_e64 v79, v10, v83, s[8:9]
	v_cndmask_b32_e64 v10, v83, v10, s[8:9]
	s_nop 1
	v_add_u32_dpp v10, v79, v10 row_half_mirror row_mask:0xf bank_mask:0xf bound_ctrl:1
	v_cndmask_b32_e64 v79, v11, v84, s[8:9]
	v_cndmask_b32_e64 v11, v84, v11, s[8:9]
	s_nop 1
	v_add_u32_dpp v11, v79, v11 row_half_mirror row_mask:0xf bank_mask:0xf bound_ctrl:1
	v_cndmask_b32_e64 v79, v12, v85, s[8:9]
	v_cndmask_b32_e64 v12, v85, v12, s[8:9]
	s_nop 1
	v_add_u32_dpp v12, v79, v12 row_half_mirror row_mask:0xf bank_mask:0xf bound_ctrl:1
	v_cndmask_b32_e64 v79, v13, v86, s[8:9]
	v_cndmask_b32_e64 v13, v86, v13, s[8:9]
	s_nop 1
	v_add_u32_dpp v13, v79, v13 row_half_mirror row_mask:0xf bank_mask:0xf bound_ctrl:1
	v_cndmask_b32_e64 v79, v78, v82, s[8:9]
	v_cndmask_b32_e64 v78, v82, v78, s[8:9]
	s_nop 1
	v_add_u32_dpp v78, v79, v78 row_half_mirror row_mask:0xf bank_mask:0xf bound_ctrl:1
	v_cndmask_b32_e64 v79, v3, v11, s[10:11]
	v_cndmask_b32_e64 v3, v11, v3, s[10:11]
	v_cndmask_b32_e64 v11, v4, v12, s[10:11]
	v_cndmask_b32_e64 v4, v12, v4, s[10:11]
	v_add_u32_dpp v3, v79, v3 quad_perm:[2,3,0,1] row_mask:0xf bank_mask:0xf bound_ctrl:1
	s_nop 0
	v_add_u32_dpp v4, v11, v4 quad_perm:[2,3,0,1] row_mask:0xf bank_mask:0xf bound_ctrl:1
	v_cndmask_b32_e64 v11, v5, v13, s[10:11]
	v_cndmask_b32_e64 v5, v13, v5, s[10:11]
	s_nop 1
	v_add_u32_dpp v5, v11, v5 quad_perm:[2,3,0,1] row_mask:0xf bank_mask:0xf bound_ctrl:1
	v_cndmask_b32_e64 v11, v10, v78, s[10:11]
	v_cndmask_b32_e64 v10, v78, v10, s[10:11]
	s_nop 1
	v_add_u32_dpp v10, v11, v10 quad_perm:[2,3,0,1] row_mask:0xf bank_mask:0xf bound_ctrl:1
	v_cndmask_b32_e64 v11, v3, v5, s[12:13]
	v_cndmask_b32_e64 v3, v5, v3, s[12:13]
	v_cndmask_b32_e64 v5, v4, v10, s[12:13]
	v_cndmask_b32_e64 v4, v10, v4, s[12:13]
	v_add_u32_dpp v3, v11, v3 quad_perm:[1,0,3,2] row_mask:0xf bank_mask:0xf bound_ctrl:1
	v_cvt_f32_i32_e32 v3, v3
	v_add_u32_dpp v4, v5, v4 quad_perm:[1,0,3,2] row_mask:0xf bank_mask:0xf bound_ctrl:1
	v_cvt_f32_i32_e32 v4, v4
	v_mov_b64_e32 v[10:11], v[18:19]
	global_store_dword v[158:159], v3, off
	global_store_dword v[158:159], v4, off offset:16
	v_lshl_add_u64 v[158:159], v[158:159], 0, s[20:21]
	v_mov_b64_e32 v[12:13], v[20:21]
	s_cbranch_vccz .LBB0_1450
